# conformer conv: pre-loop vmcnt(0) relaxed to vmcnt(4); the four norm-parameter loads are waited in front of the mid-iteration barrier, their first consumer
# baseline (speedup 1.0000x reference)
.LBB0_2163:
	s_or_b64 exec, exec, s[18:19]
	v_readlane_b32 s36, v251, 19
	v_readlane_b32 s50, v251, 33
	v_readlane_b32 s37, v251, 20
	v_readlane_b32 s38, v251, 21
	v_readlane_b32 s39, v251, 22
	v_readlane_b32 s40, v251, 23
	v_readlane_b32 s41, v251, 24
	v_readlane_b32 s42, v251, 25
	v_readlane_b32 s43, v251, 26
	v_readlane_b32 s44, v251, 27
	v_readlane_b32 s45, v251, 28
	v_readlane_b32 s46, v251, 29
	v_readlane_b32 s47, v251, 30
	v_readlane_b32 s48, v251, 31
	v_readlane_b32 s49, v251, 32
	v_readlane_b32 s51, v251, 34
	s_add_u32 s18, s50, s16
	s_addc_u32 s19, s51, s17
	v_readlane_b32 s36, v251, 35
	v_readlane_b32 s37, v251, 36
	s_add_u32 s16, s36, s16
	s_waitcnt vmcnt(32)
	v_lshlrev_b32_e32 v18, 2, v84
	s_addc_u32 s17, s37, s17
	global_load_dwordx4 v[2:5], v18, s[18:19] offset:16
	global_load_dwordx4 v[6:9], v18, s[18:19]
	global_load_dwordx4 v[10:13], v18, s[16:17] offset:16
	global_load_dwordx4 v[14:17], v18, s[16:17]
	v_ashrrev_i32_e32 v19, 5, v50
	v_or_b32_e32 v25, 1, v19
	v_readlane_b32 s2, v255, 30
	v_readlane_b32 s6, v254, 23
	s_add_i32 s4, 0, 0x18000
	v_readlane_b32 s3, v255, 31
	v_add_u32_e32 v20, s6, v25
	v_and_b32_e32 v24, -2, v19
	v_add_u32_e32 v28, s4, v18
	v_lshl_add_u64 v[18:19], s[2:3], 0, v[98:99]
	v_ashrrev_i32_e32 v21, 31, v20
	v_readlane_b32 s2, v254, 15
	v_readlane_b32 s3, v255, 18
	v_lshlrev_b64 v[20:21], 11, v[20:21]
	v_and_b32_e32 v26, 63, v50
	s_add_u32 s2, s2, s3
	v_readlane_b32 s3, v254, 16
	v_lshlrev_b32_e32 v27, 11, v24
	v_lshlrev_b32_e32 v29, 11, v25
	v_lshl_or_b32 v20, v26, 4, v20
	s_addc_u32 s3, s3, 0
	v_lshl_add_u32 v22, v50, 1, 0
	v_lshl_add_u32 v23, v50, 2, s4
	v_lshl_add_u64 v[20:21], s[2:3], 0, v[20:21]
	v_add_u32_e32 v26, s6, v24
	s_mov_b32 s36, 0
	v_add_u32_e32 v27, v28, v27
	v_add_u32_e32 v28, v28, v29
	v_readlane_b32 s38, v251, 37
	v_readlane_b32 s39, v251, 38
	v_readlane_b32 s40, v251, 39
	v_readlane_b32 s41, v251, 40
	v_readlane_b32 s42, v251, 41
	v_readlane_b32 s43, v251, 42
	v_readlane_b32 s44, v251, 43
	v_readlane_b32 s45, v251, 44
	v_readlane_b32 s46, v251, 45
	v_readlane_b32 s47, v251, 46
	v_readlane_b32 s48, v251, 47
	v_readlane_b32 s49, v251, 48
	v_readlane_b32 s50, v251, 49
	v_readlane_b32 s51, v251, 50
	s_waitcnt lgkmcnt(0)
	s_barrier
	s_waitcnt vmcnt(4)
	s_branch .LBB0_2165

.LBB0_2165:
	ds_read_u16 v29, v22
	ds_read_u16 v30, v22 offset:1024
	ds_read_u16 v31, v22 offset:2048
	ds_read_u16 v32, v22 offset:3072
	ds_read_u16 v33, v22 offset:4096
	ds_read_u16 v34, v22 offset:5120
	ds_read_u16 v35, v22 offset:6144
	ds_read_u16 v36, v22 offset:7168
	s_waitcnt lgkmcnt(7)
	v_lshlrev_b32_e32 v29, 16, v29
	v_fma_f32 v29, v51, v29, v52
	s_waitcnt lgkmcnt(6)
	v_lshlrev_b32_e32 v30, 16, v30
	v_fmac_f32_e32 v29, v54, v30
	v_fma_f32 v30, v51, v30, v52
	s_waitcnt lgkmcnt(5)
	v_lshlrev_b32_e32 v31, 16, v31
	v_fmac_f32_e32 v29, v55, v31
	v_fmac_f32_e32 v30, v54, v31
	v_fma_f32 v31, v51, v31, v52
	s_waitcnt lgkmcnt(4)
	v_lshlrev_b32_e32 v32, 16, v32
	ds_read_u16 v37, v22 offset:8192
	ds_read_u16 v38, v22 offset:9216
	ds_read_u16 v39, v22 offset:10240
	ds_read_u16 v40, v22 offset:11264
	ds_read_u16 v41, v22 offset:12288
	ds_read_u16 v42, v22 offset:13312
	ds_read_u16 v43, v22 offset:14336
	ds_read_u16 v44, v22 offset:15360
	v_fmac_f32_e32 v29, v56, v32
	v_fmac_f32_e32 v30, v55, v32
	v_fmac_f32_e32 v31, v54, v32
	v_fma_f32 v32, v51, v32, v52
	s_waitcnt lgkmcnt(11)
	v_lshlrev_b32_e32 v33, 16, v33
	v_fmac_f32_e32 v29, v57, v33
	v_fmac_f32_e32 v30, v56, v33
	v_fmac_f32_e32 v31, v55, v33
	v_fmac_f32_e32 v32, v54, v33
	v_fma_f32 v33, v51, v33, v52
	s_waitcnt lgkmcnt(10)
	v_lshlrev_b32_e32 v34, 16, v34
	v_fmac_f32_e32 v29, v58, v34
	v_fmac_f32_e32 v30, v57, v34
	v_fmac_f32_e32 v31, v56, v34
	v_fmac_f32_e32 v32, v55, v34
	v_fmac_f32_e32 v33, v54, v34
	v_fma_f32 v34, v51, v34, v52
	s_waitcnt lgkmcnt(9)
	v_lshlrev_b32_e32 v35, 16, v35
	v_fmac_f32_e32 v29, v59, v35
	v_fmac_f32_e32 v30, v58, v35
	v_fmac_f32_e32 v31, v57, v35
	v_fmac_f32_e32 v32, v56, v35
	v_fmac_f32_e32 v33, v55, v35
	v_fmac_f32_e32 v34, v54, v35
	v_fma_f32 v35, v51, v35, v52
	s_waitcnt lgkmcnt(8)
	v_lshlrev_b32_e32 v36, 16, v36
	v_fmac_f32_e32 v29, v60, v36
	v_fmac_f32_e32 v30, v59, v36
	v_fmac_f32_e32 v31, v58, v36
	v_fmac_f32_e32 v32, v57, v36
	v_fmac_f32_e32 v33, v56, v36
	v_fmac_f32_e32 v34, v55, v36
	v_fmac_f32_e32 v35, v54, v36
	v_fma_f32 v36, v51, v36, v52
	s_waitcnt lgkmcnt(7)
	v_lshlrev_b32_e32 v37, 16, v37
	v_fmac_f32_e32 v29, v61, v37
	v_fmac_f32_e32 v30, v60, v37
	v_fmac_f32_e32 v31, v59, v37
	v_fmac_f32_e32 v32, v58, v37
	v_fmac_f32_e32 v33, v57, v37
	v_fmac_f32_e32 v34, v56, v37
	v_fmac_f32_e32 v35, v55, v37
	v_fmac_f32_e32 v36, v54, v37
	v_fma_f32 v37, v51, v37, v52
	s_waitcnt lgkmcnt(6)
	v_lshlrev_b32_e32 v38, 16, v38
	v_fmac_f32_e32 v29, v62, v38
	v_fmac_f32_e32 v30, v61, v38
	v_fmac_f32_e32 v31, v60, v38
	v_fmac_f32_e32 v32, v59, v38
	v_fmac_f32_e32 v33, v58, v38
	v_fmac_f32_e32 v34, v57, v38
	v_fmac_f32_e32 v35, v56, v38
	v_fmac_f32_e32 v36, v55, v38
	v_fmac_f32_e32 v37, v54, v38
	v_fma_f32 v38, v51, v38, v52
	s_waitcnt lgkmcnt(5)
	v_lshlrev_b32_e32 v39, 16, v39
	v_fmac_f32_e32 v29, v63, v39
	v_fmac_f32_e32 v30, v62, v39
	v_fmac_f32_e32 v31, v61, v39
	v_fmac_f32_e32 v32, v60, v39
	v_fmac_f32_e32 v33, v59, v39
	v_fmac_f32_e32 v34, v58, v39
	v_fmac_f32_e32 v35, v57, v39
	v_fmac_f32_e32 v36, v56, v39
	v_fmac_f32_e32 v37, v55, v39
	v_fmac_f32_e32 v38, v54, v39
	v_fma_f32 v39, v51, v39, v52
	s_waitcnt lgkmcnt(4)
	v_lshlrev_b32_e32 v40, 16, v40
	ds_read_u16 v45, v22 offset:16384
	v_fmac_f32_e32 v29, v64, v40
	v_fmac_f32_e32 v30, v63, v40
	v_fmac_f32_e32 v31, v62, v40
	v_fmac_f32_e32 v32, v61, v40
	v_fmac_f32_e32 v33, v60, v40
	v_fmac_f32_e32 v34, v59, v40
	v_fmac_f32_e32 v35, v58, v40
	v_fmac_f32_e32 v36, v57, v40
	v_fmac_f32_e32 v37, v56, v40
	v_fmac_f32_e32 v38, v55, v40
	v_fmac_f32_e32 v39, v54, v40
	v_fma_f32 v40, v51, v40, v52
	s_waitcnt lgkmcnt(4)
	v_lshlrev_b32_e32 v41, 16, v41
	v_fmac_f32_e32 v29, v65, v41
	v_fmac_f32_e32 v30, v64, v41
	v_fmac_f32_e32 v31, v63, v41
	v_fmac_f32_e32 v32, v62, v41
	v_fmac_f32_e32 v33, v61, v41
	v_fmac_f32_e32 v34, v60, v41
	v_fmac_f32_e32 v35, v59, v41
	v_fmac_f32_e32 v36, v58, v41
	v_fmac_f32_e32 v37, v57, v41
	v_fmac_f32_e32 v38, v56, v41
	v_fmac_f32_e32 v39, v55, v41
	v_fmac_f32_e32 v40, v54, v41
	v_fma_f32 v41, v51, v41, v52
	s_waitcnt lgkmcnt(3)
	v_lshlrev_b32_e32 v42, 16, v42
	v_fmac_f32_e32 v29, v66, v42
	v_fmac_f32_e32 v30, v65, v42
	v_fmac_f32_e32 v31, v64, v42
	v_fmac_f32_e32 v32, v63, v42
	v_fmac_f32_e32 v33, v62, v42
	v_fmac_f32_e32 v34, v61, v42
	v_fmac_f32_e32 v35, v60, v42
	v_fmac_f32_e32 v36, v59, v42
	v_fmac_f32_e32 v37, v58, v42
	v_fmac_f32_e32 v38, v57, v42
	v_fmac_f32_e32 v39, v56, v42
	v_fmac_f32_e32 v40, v55, v42
	v_fmac_f32_e32 v41, v54, v42
	v_fma_f32 v42, v51, v42, v52
	s_waitcnt lgkmcnt(2)
	v_lshlrev_b32_e32 v43, 16, v43
	v_fmac_f32_e32 v29, v67, v43
	v_fmac_f32_e32 v30, v66, v43
	v_fmac_f32_e32 v31, v65, v43
	v_fmac_f32_e32 v32, v64, v43
	v_fmac_f32_e32 v33, v63, v43
	v_fmac_f32_e32 v34, v62, v43
	v_fmac_f32_e32 v35, v61, v43
	v_fmac_f32_e32 v36, v60, v43
	v_fmac_f32_e32 v37, v59, v43
	v_fmac_f32_e32 v38, v58, v43
	v_fmac_f32_e32 v39, v57, v43
	v_fmac_f32_e32 v40, v56, v43
	v_fmac_f32_e32 v41, v55, v43
	v_fmac_f32_e32 v42, v54, v43
	v_fma_f32 v43, v51, v43, v52
	s_waitcnt lgkmcnt(1)
	v_lshlrev_b32_e32 v44, 16, v44
	v_fmac_f32_e32 v29, v68, v44
	v_fmac_f32_e32 v30, v67, v44
	v_fmac_f32_e32 v31, v66, v44
	v_fmac_f32_e32 v32, v65, v44
	v_fmac_f32_e32 v33, v64, v44
	v_fmac_f32_e32 v34, v63, v44
	v_fmac_f32_e32 v35, v62, v44
	v_fmac_f32_e32 v36, v61, v44
	v_fmac_f32_e32 v37, v60, v44
	v_fmac_f32_e32 v38, v59, v44
	v_fmac_f32_e32 v39, v58, v44
	v_fmac_f32_e32 v40, v57, v44
	v_fmac_f32_e32 v41, v56, v44
	v_fmac_f32_e32 v42, v55, v44
	v_fmac_f32_e32 v43, v54, v44
	v_fma_f32 v44, v51, v44, v52
	s_waitcnt lgkmcnt(0)
	v_lshlrev_b32_e32 v45, 16, v45
	v_fmac_f32_e32 v29, v69, v45
	v_fmac_f32_e32 v30, v68, v45
	v_fmac_f32_e32 v31, v67, v45
	v_fmac_f32_e32 v32, v66, v45
	v_fmac_f32_e32 v33, v65, v45
	v_fmac_f32_e32 v34, v64, v45
	v_fmac_f32_e32 v35, v63, v45
	v_fmac_f32_e32 v36, v62, v45
	v_fmac_f32_e32 v37, v61, v45
	v_fmac_f32_e32 v38, v60, v45
	v_fmac_f32_e32 v39, v59, v45
	v_fmac_f32_e32 v40, v58, v45
	v_fmac_f32_e32 v41, v57, v45
	v_fmac_f32_e32 v42, v56, v45
	v_fmac_f32_e32 v43, v55, v45
	v_fmac_f32_e32 v44, v54, v45
	ds_read_u16 v100, v22 offset:17408
	ds_read_u16 v101, v22 offset:18432
	ds_read_u16 v102, v22 offset:19456
	ds_read_u16 v103, v22 offset:20480
	ds_read_u16 v104, v22 offset:21504
	ds_read_u16 v105, v22 offset:22528
	ds_read_u16 v106, v22 offset:23552
	ds_read_u16 v107, v22 offset:24576
	s_waitcnt lgkmcnt(7)
	v_lshlrev_b32_e32 v45, 16, v100
	ds_read_u16 v100, v22 offset:25600
	v_fmac_f32_e32 v29, v70, v45
	v_fmac_f32_e32 v30, v69, v45
	v_fmac_f32_e32 v31, v68, v45
	v_fmac_f32_e32 v32, v67, v45
	v_fmac_f32_e32 v33, v66, v45
	v_fmac_f32_e32 v34, v65, v45
	v_fmac_f32_e32 v35, v64, v45
	v_fmac_f32_e32 v36, v63, v45
	v_fmac_f32_e32 v37, v62, v45
	v_fmac_f32_e32 v38, v61, v45
	v_fmac_f32_e32 v39, v60, v45
	v_fmac_f32_e32 v40, v59, v45
	v_fmac_f32_e32 v41, v58, v45
	v_fmac_f32_e32 v42, v57, v45
	v_fmac_f32_e32 v43, v56, v45
	v_fmac_f32_e32 v44, v55, v45
	s_waitcnt lgkmcnt(7)
	v_lshlrev_b32_e32 v45, 16, v101
	ds_read_u16 v101, v22 offset:26624
	v_fmac_f32_e32 v29, v71, v45
	v_fmac_f32_e32 v30, v70, v45
	v_fmac_f32_e32 v31, v69, v45
	v_fmac_f32_e32 v32, v68, v45
	v_fmac_f32_e32 v33, v67, v45
	v_fmac_f32_e32 v34, v66, v45
	v_fmac_f32_e32 v35, v65, v45
	v_fmac_f32_e32 v36, v64, v45
	v_fmac_f32_e32 v37, v63, v45
	v_fmac_f32_e32 v38, v62, v45
	v_fmac_f32_e32 v39, v61, v45
	v_fmac_f32_e32 v40, v60, v45
	v_fmac_f32_e32 v41, v59, v45
	v_fmac_f32_e32 v42, v58, v45
	v_fmac_f32_e32 v43, v57, v45
	v_fmac_f32_e32 v44, v56, v45
	s_waitcnt lgkmcnt(7)
	v_lshlrev_b32_e32 v45, 16, v102
	ds_read_u16 v102, v22 offset:27648
	v_fmac_f32_e32 v29, v72, v45
	v_fmac_f32_e32 v30, v71, v45
	v_fmac_f32_e32 v31, v70, v45
	v_fmac_f32_e32 v32, v69, v45
	v_fmac_f32_e32 v33, v68, v45
	v_fmac_f32_e32 v34, v67, v45
	v_fmac_f32_e32 v35, v66, v45
	v_fmac_f32_e32 v36, v65, v45
	v_fmac_f32_e32 v37, v64, v45
	v_fmac_f32_e32 v38, v63, v45
	v_fmac_f32_e32 v39, v62, v45
	v_fmac_f32_e32 v40, v61, v45
	v_fmac_f32_e32 v41, v60, v45
	v_fmac_f32_e32 v42, v59, v45
	v_fmac_f32_e32 v43, v58, v45
	v_fmac_f32_e32 v44, v57, v45
	s_waitcnt lgkmcnt(7)
	v_lshlrev_b32_e32 v45, 16, v103
	ds_read_u16 v103, v22 offset:28672
	v_fmac_f32_e32 v29, v73, v45
	v_fmac_f32_e32 v30, v72, v45
	v_fmac_f32_e32 v31, v71, v45
	v_fmac_f32_e32 v32, v70, v45
	v_fmac_f32_e32 v33, v69, v45
	v_fmac_f32_e32 v34, v68, v45
	v_fmac_f32_e32 v35, v67, v45
	v_fmac_f32_e32 v36, v66, v45
	v_fmac_f32_e32 v37, v65, v45
	v_fmac_f32_e32 v38, v64, v45
	v_fmac_f32_e32 v39, v63, v45
	v_fmac_f32_e32 v40, v62, v45
	v_fmac_f32_e32 v41, v61, v45
	v_fmac_f32_e32 v42, v60, v45
	v_fmac_f32_e32 v43, v59, v45
	v_fmac_f32_e32 v44, v58, v45
	s_waitcnt lgkmcnt(7)
	v_lshlrev_b32_e32 v45, 16, v104
	ds_read_u16 v104, v22 offset:29696
	v_fmac_f32_e32 v29, v74, v45
	v_fmac_f32_e32 v30, v73, v45
	v_fmac_f32_e32 v31, v72, v45
	v_fmac_f32_e32 v32, v71, v45
	v_fmac_f32_e32 v33, v70, v45
	v_fmac_f32_e32 v34, v69, v45
	v_fmac_f32_e32 v35, v68, v45
	v_fmac_f32_e32 v36, v67, v45
	v_fmac_f32_e32 v37, v66, v45
	v_fmac_f32_e32 v38, v65, v45
	v_fmac_f32_e32 v39, v64, v45
	v_fmac_f32_e32 v40, v63, v45
	v_fmac_f32_e32 v41, v62, v45
	v_fmac_f32_e32 v42, v61, v45
	v_fmac_f32_e32 v43, v60, v45
	v_fmac_f32_e32 v44, v59, v45
	s_waitcnt lgkmcnt(7)
	v_lshlrev_b32_e32 v45, 16, v105
	ds_read_u16 v105, v22 offset:30720
	v_fmac_f32_e32 v29, v75, v45
	v_fmac_f32_e32 v30, v74, v45
	v_fmac_f32_e32 v31, v73, v45
	v_fmac_f32_e32 v32, v72, v45
	v_fmac_f32_e32 v33, v71, v45
	v_fmac_f32_e32 v34, v70, v45
	v_fmac_f32_e32 v35, v69, v45
	v_fmac_f32_e32 v36, v68, v45
	v_fmac_f32_e32 v37, v67, v45
	v_fmac_f32_e32 v38, v66, v45
	v_fmac_f32_e32 v39, v65, v45
	v_fmac_f32_e32 v40, v64, v45
	v_fmac_f32_e32 v41, v63, v45
	v_fmac_f32_e32 v42, v62, v45
	v_fmac_f32_e32 v43, v61, v45
	v_fmac_f32_e32 v44, v60, v45
	s_waitcnt lgkmcnt(7)
	v_lshlrev_b32_e32 v45, 16, v106
	ds_read_u16 v106, v22 offset:31744
	v_fmac_f32_e32 v29, v76, v45
	v_fmac_f32_e32 v30, v75, v45
	v_fmac_f32_e32 v31, v74, v45
	v_fmac_f32_e32 v32, v73, v45
	v_fmac_f32_e32 v33, v72, v45
	v_fmac_f32_e32 v34, v71, v45
	v_fmac_f32_e32 v35, v70, v45
	v_fmac_f32_e32 v36, v69, v45
	v_fmac_f32_e32 v37, v68, v45
	v_fmac_f32_e32 v38, v67, v45
	v_fmac_f32_e32 v39, v66, v45
	v_fmac_f32_e32 v40, v65, v45
	v_fmac_f32_e32 v41, v64, v45
	v_fmac_f32_e32 v42, v63, v45
	v_fmac_f32_e32 v43, v62, v45
	v_fmac_f32_e32 v44, v61, v45
	s_waitcnt lgkmcnt(7)
	v_lshlrev_b32_e32 v45, 16, v107
	ds_read_u16 v107, v22 offset:32768
	v_fmac_f32_e32 v29, v77, v45
	v_fmac_f32_e32 v30, v76, v45
	v_fmac_f32_e32 v31, v75, v45
	v_fmac_f32_e32 v32, v74, v45
	v_fmac_f32_e32 v33, v73, v45
	v_fmac_f32_e32 v34, v72, v45
	v_fmac_f32_e32 v35, v71, v45
	v_fmac_f32_e32 v36, v70, v45
	v_fmac_f32_e32 v37, v69, v45
	v_fmac_f32_e32 v38, v68, v45
	v_fmac_f32_e32 v39, v67, v45
	v_fmac_f32_e32 v40, v66, v45
	v_fmac_f32_e32 v41, v65, v45
	v_fmac_f32_e32 v42, v64, v45
	v_fmac_f32_e32 v43, v63, v45
	v_fmac_f32_e32 v44, v62, v45
	s_waitcnt lgkmcnt(7)
	v_lshlrev_b32_e32 v45, 16, v100
	ds_read_u16 v100, v22 offset:33792
	v_fmac_f32_e32 v29, v78, v45
	v_fmac_f32_e32 v30, v77, v45
	v_fmac_f32_e32 v31, v76, v45
	v_fmac_f32_e32 v32, v75, v45
	v_fmac_f32_e32 v33, v74, v45
	v_fmac_f32_e32 v34, v73, v45
	v_fmac_f32_e32 v35, v72, v45
	v_fmac_f32_e32 v36, v71, v45
	v_fmac_f32_e32 v37, v70, v45
	v_fmac_f32_e32 v38, v69, v45
	v_fmac_f32_e32 v39, v68, v45
	v_fmac_f32_e32 v40, v67, v45
	v_fmac_f32_e32 v41, v66, v45
	v_fmac_f32_e32 v42, v65, v45
	v_fmac_f32_e32 v43, v64, v45
	v_fmac_f32_e32 v44, v63, v45
	s_waitcnt lgkmcnt(7)
	v_lshlrev_b32_e32 v45, 16, v101
	ds_read_u16 v101, v22 offset:34816
	v_fmac_f32_e32 v29, v79, v45
	v_fmac_f32_e32 v30, v78, v45
	v_fmac_f32_e32 v31, v77, v45
	v_fmac_f32_e32 v32, v76, v45
	v_fmac_f32_e32 v33, v75, v45
	v_fmac_f32_e32 v34, v74, v45
	v_fmac_f32_e32 v35, v73, v45
	v_fmac_f32_e32 v36, v72, v45
	v_fmac_f32_e32 v37, v71, v45
	v_fmac_f32_e32 v38, v70, v45
	v_fmac_f32_e32 v39, v69, v45
	v_fmac_f32_e32 v40, v68, v45
	v_fmac_f32_e32 v41, v67, v45
	v_fmac_f32_e32 v42, v66, v45
	v_fmac_f32_e32 v43, v65, v45
	v_fmac_f32_e32 v44, v64, v45
	s_waitcnt lgkmcnt(7)
	v_lshlrev_b32_e32 v45, 16, v102
	ds_read_u16 v102, v22 offset:35840
	v_fmac_f32_e32 v29, v80, v45
	v_fmac_f32_e32 v30, v79, v45
	v_fmac_f32_e32 v31, v78, v45
	v_fmac_f32_e32 v32, v77, v45
	v_fmac_f32_e32 v33, v76, v45
	v_fmac_f32_e32 v34, v75, v45
	v_fmac_f32_e32 v35, v74, v45
	v_fmac_f32_e32 v36, v73, v45
	v_fmac_f32_e32 v37, v72, v45
	v_fmac_f32_e32 v38, v71, v45
	v_fmac_f32_e32 v39, v70, v45
	v_fmac_f32_e32 v40, v69, v45
	v_fmac_f32_e32 v41, v68, v45
	v_fmac_f32_e32 v42, v67, v45
	v_fmac_f32_e32 v43, v66, v45
	v_fmac_f32_e32 v44, v65, v45
	s_waitcnt lgkmcnt(7)
	v_lshlrev_b32_e32 v45, 16, v103
	ds_read_u16 v103, v22 offset:36864
	v_fmac_f32_e32 v29, v81, v45
	v_fmac_f32_e32 v30, v80, v45
	v_fmac_f32_e32 v31, v79, v45
	v_fmac_f32_e32 v32, v78, v45
	v_fmac_f32_e32 v33, v77, v45
	v_fmac_f32_e32 v34, v76, v45
	v_fmac_f32_e32 v35, v75, v45
	v_fmac_f32_e32 v36, v74, v45
	v_fmac_f32_e32 v37, v73, v45
	v_fmac_f32_e32 v38, v72, v45
	v_fmac_f32_e32 v39, v71, v45
	v_fmac_f32_e32 v40, v70, v45
	v_fmac_f32_e32 v41, v69, v45
	v_fmac_f32_e32 v42, v68, v45
	v_fmac_f32_e32 v43, v67, v45
	v_fmac_f32_e32 v44, v66, v45
	s_waitcnt lgkmcnt(7)
	v_lshlrev_b32_e32 v45, 16, v104
	ds_read_u16 v104, v22 offset:37888
	v_fmac_f32_e32 v29, v82, v45
	v_fmac_f32_e32 v30, v81, v45
	v_fmac_f32_e32 v31, v80, v45
	v_fmac_f32_e32 v32, v79, v45
	v_fmac_f32_e32 v33, v78, v45
	v_fmac_f32_e32 v34, v77, v45
	v_fmac_f32_e32 v35, v76, v45
	v_fmac_f32_e32 v36, v75, v45
	v_fmac_f32_e32 v37, v74, v45
	v_fmac_f32_e32 v38, v73, v45
	v_fmac_f32_e32 v39, v72, v45
	v_fmac_f32_e32 v40, v71, v45
	v_fmac_f32_e32 v41, v70, v45
	v_fmac_f32_e32 v42, v69, v45
	v_fmac_f32_e32 v43, v68, v45
	v_fmac_f32_e32 v44, v67, v45
	s_waitcnt lgkmcnt(7)
	v_lshlrev_b32_e32 v45, 16, v105
	ds_read_u16 v105, v22 offset:38912
	v_fmac_f32_e32 v29, v83, v45
	v_fmac_f32_e32 v30, v82, v45
	v_fmac_f32_e32 v31, v81, v45
	v_fmac_f32_e32 v32, v80, v45
	v_fmac_f32_e32 v33, v79, v45
	v_fmac_f32_e32 v34, v78, v45
	v_fmac_f32_e32 v35, v77, v45
	v_fmac_f32_e32 v36, v76, v45
	v_fmac_f32_e32 v37, v75, v45
	v_fmac_f32_e32 v38, v74, v45
	v_fmac_f32_e32 v39, v73, v45
	v_fmac_f32_e32 v40, v72, v45
	v_fmac_f32_e32 v41, v71, v45
	v_fmac_f32_e32 v42, v70, v45
	v_fmac_f32_e32 v43, v69, v45
	v_fmac_f32_e32 v44, v68, v45
	s_waitcnt lgkmcnt(7)
	v_lshlrev_b32_e32 v45, 16, v106
	ds_read_u16 v106, v22 offset:39936
	v_fmac_f32_e32 v30, v83, v45
	v_fmac_f32_e32 v31, v82, v45
	v_fmac_f32_e32 v32, v81, v45
	v_fmac_f32_e32 v33, v80, v45
	v_fmac_f32_e32 v34, v79, v45
	v_fmac_f32_e32 v35, v78, v45
	v_fmac_f32_e32 v36, v77, v45
	v_fmac_f32_e32 v37, v76, v45
	v_fmac_f32_e32 v38, v75, v45
	v_fmac_f32_e32 v39, v74, v45
	v_fmac_f32_e32 v40, v73, v45
	v_fmac_f32_e32 v41, v72, v45
	v_fmac_f32_e32 v42, v71, v45
	v_fmac_f32_e32 v43, v70, v45
	v_fmac_f32_e32 v44, v69, v45
	s_waitcnt lgkmcnt(7)
	v_lshlrev_b32_e32 v45, 16, v107
	ds_read_u16 v107, v22 offset:40960
	v_fmac_f32_e32 v31, v83, v45
	v_fmac_f32_e32 v32, v82, v45
	v_fmac_f32_e32 v33, v81, v45
	v_fmac_f32_e32 v34, v80, v45
	v_fmac_f32_e32 v35, v79, v45
	v_fmac_f32_e32 v36, v78, v45
	v_fmac_f32_e32 v37, v77, v45
	v_fmac_f32_e32 v38, v76, v45
	v_fmac_f32_e32 v39, v75, v45
	v_fmac_f32_e32 v40, v74, v45
	v_fmac_f32_e32 v41, v73, v45
	v_fmac_f32_e32 v42, v72, v45
	v_fmac_f32_e32 v43, v71, v45
	v_fmac_f32_e32 v44, v70, v45
	s_waitcnt lgkmcnt(7)
	v_lshlrev_b32_e32 v45, 16, v100
	ds_read_u16 v100, v22 offset:41984
	v_fmac_f32_e32 v32, v83, v45
	v_fmac_f32_e32 v33, v82, v45
	v_fmac_f32_e32 v34, v81, v45
	v_fmac_f32_e32 v35, v80, v45
	v_fmac_f32_e32 v36, v79, v45
	v_fmac_f32_e32 v37, v78, v45
	v_fmac_f32_e32 v38, v77, v45
	v_fmac_f32_e32 v39, v76, v45
	v_fmac_f32_e32 v40, v75, v45
	v_fmac_f32_e32 v41, v74, v45
	v_fmac_f32_e32 v42, v73, v45
	v_fmac_f32_e32 v43, v72, v45
	v_fmac_f32_e32 v44, v71, v45
	s_waitcnt lgkmcnt(7)
	v_lshlrev_b32_e32 v45, 16, v101
	ds_read_u16 v101, v22 offset:43008
	v_fmac_f32_e32 v33, v83, v45
	v_fmac_f32_e32 v34, v82, v45
	v_fmac_f32_e32 v35, v81, v45
	v_fmac_f32_e32 v36, v80, v45
	v_fmac_f32_e32 v37, v79, v45
	v_fmac_f32_e32 v38, v78, v45
	v_fmac_f32_e32 v39, v77, v45
	v_fmac_f32_e32 v40, v76, v45
	v_fmac_f32_e32 v41, v75, v45
	v_fmac_f32_e32 v42, v74, v45
	v_fmac_f32_e32 v43, v73, v45
	v_fmac_f32_e32 v44, v72, v45
	s_waitcnt lgkmcnt(7)
	v_lshlrev_b32_e32 v45, 16, v102
	ds_read_u16 v102, v22 offset:44032
	v_fmac_f32_e32 v34, v83, v45
	v_fmac_f32_e32 v35, v82, v45
	v_fmac_f32_e32 v36, v81, v45
	v_fmac_f32_e32 v37, v80, v45
	v_fmac_f32_e32 v38, v79, v45
	v_fmac_f32_e32 v39, v78, v45
	v_fmac_f32_e32 v40, v77, v45
	v_fmac_f32_e32 v41, v76, v45
	v_fmac_f32_e32 v42, v75, v45
	v_fmac_f32_e32 v43, v74, v45
	v_fmac_f32_e32 v44, v73, v45
	s_waitcnt lgkmcnt(7)
	v_lshlrev_b32_e32 v45, 16, v103
	ds_read_u16 v103, v22 offset:45056
	v_fmac_f32_e32 v35, v83, v45
	v_fmac_f32_e32 v36, v82, v45
	v_fmac_f32_e32 v37, v81, v45
	v_fmac_f32_e32 v38, v80, v45
	v_fmac_f32_e32 v39, v79, v45
	v_fmac_f32_e32 v40, v78, v45
	v_fmac_f32_e32 v41, v77, v45
	v_fmac_f32_e32 v42, v76, v45
	v_fmac_f32_e32 v43, v75, v45
	v_fmac_f32_e32 v44, v74, v45
	s_waitcnt lgkmcnt(7)
	v_lshlrev_b32_e32 v45, 16, v104
	ds_read_u16 v104, v22 offset:46080
	v_fmac_f32_e32 v36, v83, v45
	v_fmac_f32_e32 v37, v82, v45
	v_fmac_f32_e32 v38, v81, v45
	v_fmac_f32_e32 v39, v80, v45
	v_fmac_f32_e32 v40, v79, v45
	v_fmac_f32_e32 v41, v78, v45
	v_fmac_f32_e32 v42, v77, v45
	v_fmac_f32_e32 v43, v76, v45
	v_fmac_f32_e32 v44, v75, v45
	s_waitcnt lgkmcnt(7)
	v_lshlrev_b32_e32 v45, 16, v105
	v_fmac_f32_e32 v37, v83, v45
	v_fmac_f32_e32 v38, v82, v45
	v_fmac_f32_e32 v39, v81, v45
	v_fmac_f32_e32 v40, v80, v45
	v_fmac_f32_e32 v41, v79, v45
	v_fmac_f32_e32 v42, v78, v45
	v_fmac_f32_e32 v43, v77, v45
	v_fmac_f32_e32 v44, v76, v45
	s_waitcnt lgkmcnt(6)
	v_lshlrev_b32_e32 v45, 16, v106
	v_fmac_f32_e32 v38, v83, v45
	v_fmac_f32_e32 v39, v82, v45
	v_fmac_f32_e32 v40, v81, v45
	v_fmac_f32_e32 v41, v80, v45
	v_fmac_f32_e32 v42, v79, v45
	v_fmac_f32_e32 v43, v78, v45
	v_fmac_f32_e32 v44, v77, v45
	s_waitcnt lgkmcnt(5)
	v_lshlrev_b32_e32 v45, 16, v107
	v_fmac_f32_e32 v39, v83, v45
	v_fmac_f32_e32 v40, v82, v45
	v_fmac_f32_e32 v41, v81, v45
	v_fmac_f32_e32 v42, v80, v45
	v_fmac_f32_e32 v43, v79, v45
	v_fmac_f32_e32 v44, v78, v45
	s_waitcnt lgkmcnt(4)
	v_lshlrev_b32_e32 v45, 16, v100
	v_fmac_f32_e32 v40, v83, v45
	v_fmac_f32_e32 v41, v82, v45
	v_fmac_f32_e32 v42, v81, v45
	v_fmac_f32_e32 v43, v80, v45
	v_fmac_f32_e32 v44, v79, v45
	s_waitcnt lgkmcnt(3)
	v_lshlrev_b32_e32 v45, 16, v101
	v_fmac_f32_e32 v41, v83, v45
	v_fmac_f32_e32 v42, v82, v45
	v_fmac_f32_e32 v43, v81, v45
	v_fmac_f32_e32 v44, v80, v45
	s_waitcnt lgkmcnt(2)
	v_lshlrev_b32_e32 v45, 16, v102
	v_fmac_f32_e32 v42, v83, v45
	v_fmac_f32_e32 v43, v82, v45
	v_fmac_f32_e32 v44, v81, v45
	s_waitcnt lgkmcnt(1)
	v_lshlrev_b32_e32 v45, 16, v103
	v_fmac_f32_e32 v43, v83, v45
	v_fmac_f32_e32 v44, v82, v45
	s_waitcnt lgkmcnt(0)
	v_lshlrev_b32_e32 v45, 16, v104
	v_fmac_f32_e32 v44, v83, v45
	ds_write2st64_b32 v23, v29, v30 offset1:8
	ds_write2st64_b32 v23, v31, v32 offset0:16 offset1:24
	ds_write2st64_b32 v23, v33, v34 offset0:32 offset1:40
	ds_write2st64_b32 v23, v35, v36 offset0:48 offset1:56
	ds_write2st64_b32 v23, v37, v38 offset0:64 offset1:72
	ds_write2st64_b32 v23, v39, v40 offset0:80 offset1:88
	ds_write2st64_b32 v23, v41, v42 offset0:96 offset1:104
	ds_write2st64_b32 v23, v43, v44 offset0:112 offset1:120
	v_add_u32_e32 v29, s36, v24
	v_cmp_gt_i32_e32 vcc, 64, v29
	s_waitcnt vmcnt(0)
	s_waitcnt lgkmcnt(0)
	s_barrier
	s_and_saveexec_b64 s[34:35], vcc
	s_cbranch_execz .LBB0_2167
	ds_read_b128 v[30:33], v27
	ds_read_b128 v[34:37], v27 offset:16
	s_waitcnt lgkmcnt(1)
	v_mov_b32_e32 v38, v31
	v_mov_b32_e32 v39, v32
	v_mov_b32_e32 v40, v30
	v_mov_b32_e32 v41, v33
	v_pk_add_f32 v[38:39], v[38:39], v[40:41]
	s_waitcnt lgkmcnt(0)
	v_mov_b32_e32 v40, v36
	v_mov_b32_e32 v41, v34
	v_mov_b32_e32 v42, v37
	v_mov_b32_e32 v43, v35
	v_pk_add_f32 v[40:41], v[40:41], v[42:43]
	v_add_f32_e32 v29, v38, v39
	v_add_f32_e32 v29, v29, v41
	v_add_f32_e32 v29, v40, v29
	v_and_b32_e32 v39, 64, v214
	v_xor_b32_e32 v38, 16, v214
	v_add_f32_dpp v29, v29, v29 quad_perm:[1,0,3,2] row_mask:0xf bank_mask:0xf bound_ctrl:1
	v_add_u32_e32 v39, 64, v39
	v_cmp_lt_i32_e32 vcc, v38, v39
	v_add_f32_dpp v29, v29, v29 quad_perm:[2,3,0,1] row_mask:0xf bank_mask:0xf bound_ctrl:1
	s_nop 0
	v_cndmask_b32_e32 v38, v214, v38, vcc
	v_add_f32_dpp v29, v29, v29 row_half_mirror row_mask:0xf bank_mask:0xf bound_ctrl:1
	v_lshlrev_b32_e32 v46, 2, v38
	s_nop 0
	v_add_f32_dpp v29, v29, v29 row_mirror row_mask:0xf bank_mask:0xf bound_ctrl:1
	ds_bpermute_b32 v38, v46, v29
	s_waitcnt lgkmcnt(0)
	v_add_f32_e32 v29, v29, v38
	v_xor_b32_e32 v38, 32, v214
	v_cmp_lt_i32_e32 vcc, v38, v39
	s_nop 1
	v_cndmask_b32_e32 v38, v214, v38, vcc
	v_lshlrev_b32_e32 v47, 2, v38
	ds_bpermute_b32 v38, v47, v29
	s_waitcnt lgkmcnt(0)
	v_add_f32_e32 v29, v29, v38
	v_fmamk_f32 v31, v29, 0xbb000000, v31
	v_fmamk_f32 v30, v29, 0xbb000000, v30
	v_fmamk_f32 v33, v29, 0xbb000000, v33
	v_fmac_f32_e32 v32, 0xbb000000, v29
	v_pk_mul_f32 v[38:39], v[32:33], v[32:33]
	v_pk_mul_f32 v[40:41], v[30:31], v[30:31]
	v_fmamk_f32 v35, v29, 0xbb000000, v35
	v_fmamk_f32 v34, v29, 0xbb000000, v34
	v_fmamk_f32 v37, v29, 0xbb000000, v37
	v_fmac_f32_e32 v36, 0xbb000000, v29
	v_pk_mov_b32 v[42:43], v[40:41], v[38:39] op_sel:[1,0]
	v_mov_b32_e32 v41, v39
	v_pk_add_f32 v[38:39], v[42:43], v[40:41]
	v_pk_mul_f32 v[40:41], v[36:37], v[36:37]
	v_pk_mul_f32 v[42:43], v[34:35], v[34:35]
	v_mov_b32_e32 v44, v40
	v_mov_b32_e32 v45, v42
	v_mov_b32_e32 v42, v41
	v_pk_add_f32 v[40:41], v[44:45], v[42:43]
	v_add_f32_e32 v29, v38, v39
	v_add_f32_e32 v29, v41, v29
	v_add_f32_e32 v29, v40, v29
	s_nop 1
	v_add_f32_dpp v29, v29, v29 quad_perm:[1,0,3,2] row_mask:0xf bank_mask:0xf bound_ctrl:1
	s_nop 1
	v_add_f32_dpp v29, v29, v29 quad_perm:[2,3,0,1] row_mask:0xf bank_mask:0xf bound_ctrl:1
	s_nop 1
	v_add_f32_dpp v29, v29, v29 row_half_mirror row_mask:0xf bank_mask:0xf bound_ctrl:1
	s_nop 1
	v_add_f32_dpp v29, v29, v29 row_mirror row_mask:0xf bank_mask:0xf bound_ctrl:1
	ds_bpermute_b32 v38, v46, v29
	s_waitcnt lgkmcnt(0)
	v_add_f32_e32 v29, v29, v38
	ds_bpermute_b32 v38, v47, v29
	s_waitcnt lgkmcnt(0)
	v_add_f32_e32 v29, v29, v38
	v_fmamk_f32 v29, v29, 0x3b000000, v1
	v_mul_f32_e32 v38, 0x4b800000, v29
	v_cmp_gt_f32_e32 vcc, s77, v29
	s_nop 1
	v_cndmask_b32_e32 v29, v29, v38, vcc
	v_rsq_f32_e32 v29, v29
	s_nop 0
	v_mul_f32_e32 v38, 0x45800000, v29
	v_cndmask_b32_e32 v38, v29, v38, vcc
	v_pk_mul_f32 v[30:31], v[30:31], v[38:39] op_sel_hi:[1,0]
	v_pk_mul_f32 v[34:35], v[34:35], v[38:39] op_sel_hi:[1,0]
	v_pk_fma_f32 v[30:31], v[6:7], v[30:31], v[14:15]
	v_pk_fma_f32 v[34:35], v[2:3], v[34:35], v[10:11]
	v_mul_f32_e32 v29, 0xbfb8aa3b, v30
	v_pk_mul_f32 v[32:33], v[32:33], v[38:39] op_sel_hi:[1,0]
	v_pk_mul_f32 v[36:37], v[36:37], v[38:39] op_sel_hi:[1,0]
	v_exp_f32_e32 v29, v29
	v_mul_f32_e32 v38, 0xbfb8aa3b, v34
	v_exp_f32_e32 v39, v38
	v_mul_f32_e32 v40, 0xbfb8aa3b, v35
	v_add_f32_e32 v29, 1.0, v29
	v_rcp_f32_e32 v38, v29
	v_add_f32_e32 v29, 1.0, v39
	v_mul_f32_e32 v39, 0xbfb8aa3b, v31
	v_exp_f32_e32 v39, v39
	v_exp_f32_e32 v41, v40
	v_pk_fma_f32 v[32:33], v[8:9], v[32:33], v[16:17]
	v_rcp_f32_e32 v40, v29
	v_add_f32_e32 v29, 1.0, v39
	v_pk_fma_f32 v[36:37], v[4:5], v[36:37], v[12:13]
	v_rcp_f32_e32 v39, v29
	v_add_f32_e32 v29, 1.0, v41
	v_mul_f32_e32 v41, 0xbfb8aa3b, v32
	v_exp_f32_e32 v42, v41
	v_mul_f32_e32 v41, 0xbfb8aa3b, v36
	v_exp_f32_e32 v43, v41
	v_rcp_f32_e32 v41, v29
	v_add_f32_e32 v29, 1.0, v42
	v_rcp_f32_e32 v42, v29
	v_add_f32_e32 v29, 1.0, v43
	v_mul_f32_e32 v43, 0xbfb8aa3b, v33
	v_exp_f32_e32 v43, v43
	v_mul_f32_e32 v44, 0xbfb8aa3b, v37
	v_exp_f32_e32 v45, v44
	v_rcp_f32_e32 v44, v29
	v_add_f32_e32 v29, 1.0, v43
	v_rcp_f32_e32 v43, v29
	v_add_f32_e32 v29, 1.0, v45
	v_rcp_f32_e32 v45, v29
	v_pk_mul_f32 v[30:31], v[30:31], v[38:39]
	v_pk_mul_f32 v[34:35], v[34:35], v[40:41]
	v_pk_mul_f32 v[32:33], v[32:33], v[42:43]
	v_cvt_pk_bf16_f32 v30, v30, v31
	v_cvt_pk_bf16_f32 v31, v32, v33
	v_cvt_pk_bf16_f32 v32, v34, v35
	v_add_u32_e32 v34, s36, v26
	v_ashrrev_i32_e32 v35, 31, v34
	v_pk_mul_f32 v[36:37], v[36:37], v[44:45]
	v_lshlrev_b64 v[34:35], 11, v[34:35]
	v_cvt_pk_bf16_f32 v33, v36, v37
	v_lshl_add_u64 v[34:35], v[18:19], 0, v[34:35]
	global_store_dwordx4 v[34:35], v[30:33], off offset:1024
